# P4 emit pass, non-diagonal tiles: scores classified against per-query float thresholds (exact histogram-bin edges, zero-bin case selected per tile) instead of recomputing every score's bin; ~12 instea
# speedup vs baseline: 1.0112x; 1.0074x over previous
; #define LAS __attribute__((address_space(3)))
; __device__ __forceinline__ int bin2(float sv, int zi) {
;     const unsigned u = __float_as_uint(sv);
;     int c = (int)((u >> 20) & 0x7FFu) - 832;
;     c = c < 0 ? 0 : (c > 207 ? 207 : c);
;     int b = (u >> 31) ? (207 - c) : (272 + c);
;     if (sv == 0.0f) b = 208 + zi;
;     return b;
; }
; template <int STAGE>
; __device__ __forceinline__ void pass2(LAS unsigned char* lds, const bf16* kbase, int g, int t0, const bf16x8 (&qf)[4][4], const f32x4 lo4, const f32x4 hi4, int wave, int r, int h2) {
;     LAS unsigned* hist = (LAS unsigned*)(lds + OFF2_HIST);
;     LAS unsigned long long* cand = (LAS unsigned long long*)(lds + OFF2_CAND);
;     LAS unsigned* gtm = (LAS unsigned*)(lds + OFF2_GT);
;     LAS unsigned* cntp = (LAS unsigned*)(lds + OFF2_CNT);
;     const int tq = t0 + r;
;     const int tb = (STAGE == 1) ? ((const LAS int*)(lds + OFF2_TB))[r] : 0;
;     bf16x8 kf[4], kn[4];
;     const bf16* kp = kbase + (size_t)r * Y0P + 8 * h2;
.LBB0_822:
	s_or_b64 exec, exec, s[4:5]
	s_andn2_b64 vcc, exec, s[82:83]
	s_waitcnt lgkmcnt(0)
	s_barrier
	s_cbranch_vccnz .LBB0_880
	v_lshl_add_u64 v[0:1], v[178:179], 0, s[36:37]
	global_load_dwordx4 v[140:143], v[0:1], off
	global_load_dwordx4 v[136:139], v[0:1], off offset:32
	global_load_dwordx4 v[132:135], v[0:1], off offset:64
	global_load_dwordx4 v[128:131], v[0:1], off offset:96
	v_lshlrev_b32_e32 v0, 2, v218
	v_add_u32_e32 v1, 0, v0
	v_add_u32_e32 v1, 0x18100, v1
	ds_read_b32 v222, v1
	s_add_i32 s0, 0, 0x18200
	v_lshlrev_b32_e32 v1, 9, v219
	v_lshlrev_b32_e32 v2, 4, v218
	v_add_u32_e32 v224, s0, v0
	v_mov_b32_e32 v0, s27
	v_add3_u32 v223, s65, v1, v2
	v_lshlrev_b32_e32 v219, 2, v219
	v_lshl_add_u32 v225, v218, 11, 0
	v_cmp_gt_u32_e64 s[84:85], 32, v217
	v_mad_u32_u24 v217, v218, s24, v0
	v_readlane_b32 s0, v254, 24
	s_waitcnt lgkmcnt(0)
	v_sub_u32_e32 v0, 0xcf, v222
	v_add_u32_e32 v0, 0x340, v0
	v_lshlrev_b32_e32 v0, 20, v0
	v_add_u32_e32 v0, 0x7fffffff, v0
	v_add_u32_e32 v1, 0x100000, v0
	v_add_u32_e32 v2, 0x230, v222
	v_lshlrev_b32_e32 v2, 20, v2
	v_add_u32_e32 v3, 0x100000, v2
	v_mov_b32_e32 v4, 0xff800000
	v_bfrev_b32_e32 v5, 1
	v_mov_b32_e32 v6, 1
	v_mov_b32_e32 v7, 0x7fc00000
	v_mov_b32_e32 v8, 0x7fffffff
	v_cmp_gt_i32_e32 vcc, 0, v222
	s_nop 1
	v_cndmask_b32_e32 v252, v0, v4, vcc
	v_cmp_eq_u32_e32 vcc, 0xcf, v222
	s_nop 1
	v_cndmask_b32_e32 v252, v252, v5, vcc
	v_cmp_lt_i32_e32 vcc, 0xcf, v222
	s_nop 1
	v_cndmask_b32_e32 v252, v252, v6, vcc
	v_cmp_lt_i32_e32 vcc, 0x10f, v222
	s_nop 1
	v_cndmask_b32_e32 v252, v252, v3, vcc
	v_cmp_eq_u32_e32 vcc, 0x1df, v222
	s_nop 1
	v_cndmask_b32_e32 v252, v252, v7, vcc
	v_cmp_gt_i32_e32 vcc, 1, v222
	s_nop 1
	v_cndmask_b32_e32 v253, v1, v4, vcc
	v_cmp_lt_i32_e32 vcc, 0xcf, v222
	s_nop 1
	v_cndmask_b32_e32 v253, v253, v6, vcc
	v_cmp_lt_i32_e32 vcc, 0x110, v222
	s_nop 1
	v_cndmask_b32_e32 v253, v253, v2, vcc
	v_cmp_lt_i32_e32 vcc, 0xcf, v222
	s_nop 1
	v_cndmask_b32_e32 v232, v8, v222, vcc
	v_cmp_lt_i32_e32 vcc, 0x10f, v222
	s_nop 1
	v_cndmask_b32_e32 v232, v232, v8, vcc

; __device__ __forceinline__ int crow(int reg, int h) { return (reg & 3) + 8 * (reg >> 2) + 4 * h; }
; template <int STAGE>
; __device__ __forceinline__ void pass2(LAS unsigned char* lds, const bf16* kbase, int g, int t0, const bf16x8 (&qf)[4][4], const f32x4 lo4, const f32x4 hi4, int wave, int r, int h2) {
;     ...
;         f32x16 acc[4];
; #pragma unroll
;         for (int hd = 0; hd < 4; ++hd) {
;             acc[hd] = f32x16{};
; #pragma unroll
;             for (int s = 0; s < 4; ++s) acc[hd] = __builtin_amdgcn_mfma_f32_32x32x16_bf16(WN ? kn[s] : kf[s], qf[hd][s], acc[hd], 0, 0, 0);
;         }
;         const int zi = (8191 - 32 * kt) >> 7;
;         const int lim = tq - 32 * kt - 4 * h2;
;         unsigned gtw = 0u, eqw = 0u;
;         float svq[16];
; #pragma unroll
;         for (int rg = 0; rg < 16; ++rg) {
;             const int c0 = att::crow(rg, 0);
;             float sv = fsum4_s(__builtin_amdgcn_fmed3f(acc[0][rg], lo4.x, hi4.x), __builtin_amdgcn_fmed3f(acc[1][rg], lo4.y, hi4.y),
;                                __builtin_amdgcn_fmed3f(acc[2][rg], lo4.z, hi4.z), __builtin_amdgcn_fmed3f(acc[3][rg], lo4.w, hi4.w));
;             const int b = bin2(sv, zi);
;             const bool valid = !DIAG || c0 <= lim;
;             if (STAGE == 0) {
;                 atomicAdd((unsigned*)&hist[r * HROW2 + (valid ? b : NB2)], 1u);
;             } else {
;                 if (valid && b > tb) gtw |= 1u << c0;
;                 if (valid && b == tb) eqw |= 1u << c0;
;                 svq[rg] = sv;
;             }
;         }
.LBB0_826:
	s_cmp_lg_u32 s0, s64
	s_cbranch_scc0 .LBB0_852
	s_waitcnt vmcnt(3)
	v_mfma_f32_32x32x16_bf16 v[0:15], v[140:143], v[64:67], 0
	s_lshl_b32 s6, s0, 5
	s_sub_i32 s7, 0x1fe0, s6
	s_lshr_b32 s7, s7, 7
	s_addk_i32 s7, 0xd0
	v_mfma_f32_32x32x16_bf16 v[16:31], v[140:143], v[80:83], 0
	v_mfma_f32_32x32x16_bf16 v[32:47], v[140:143], v[96:99], 0
	v_mfma_f32_32x32x16_bf16 v[48:63], v[140:143], v[112:115], 0
	s_waitcnt vmcnt(2)
	v_mfma_f32_32x32x16_bf16 v[0:15], v[136:139], v[68:71], v[0:15]
	v_mfma_f32_32x32x16_bf16 v[16:31], v[136:139], v[84:87], v[16:31]
	v_mfma_f32_32x32x16_bf16 v[32:47], v[136:139], v[100:103], v[32:47]
	v_mfma_f32_32x32x16_bf16 v[48:63], v[136:139], v[116:119], v[48:63]
	s_waitcnt vmcnt(1)
	v_mfma_f32_32x32x16_bf16 v[0:15], v[132:135], v[72:75], v[0:15]
	v_mfma_f32_32x32x16_bf16 v[16:31], v[132:135], v[88:91], v[16:31]
	v_mfma_f32_32x32x16_bf16 v[32:47], v[132:135], v[104:107], v[32:47]
	v_mfma_f32_32x32x16_bf16 v[48:63], v[132:135], v[120:123], v[48:63]
	s_waitcnt vmcnt(0)
	v_mfma_f32_32x32x16_bf16 v[0:15], v[128:131], v[76:79], v[0:15]
	v_mfma_f32_32x32x16_bf16 v[16:31], v[128:131], v[92:95], v[16:31]
	v_mfma_f32_32x32x16_bf16 v[32:47], v[128:131], v[108:111], v[32:47]
	v_mfma_f32_32x32x16_bf16 v[48:63], v[128:131], v[124:127], v[48:63]
	v_cmp_gt_i32_e32 vcc, s7, v232
	v_cmp_ge_i32_e64 s[98:99], s7, v232
	s_nop 6
	v_cndmask_b32_e32 v250, v252, v177, vcc
	v_cndmask_b32_e64 v251, v253, v177, s[98:99]
	v_med3_f32 v0, v0, v207, v208
	v_med3_f32 v1, v1, v207, v208
	v_med3_f32 v2, v2, v207, v208
	v_med3_f32 v3, v3, v207, v208
	v_med3_f32 v4, v4, v207, v208
	v_med3_f32 v5, v5, v207, v208
	v_med3_f32 v6, v6, v207, v208
	v_med3_f32 v7, v7, v207, v208
	v_med3_f32 v8, v8, v207, v208
	v_med3_f32 v9, v9, v207, v208
	v_med3_f32 v10, v10, v207, v208
	v_med3_f32 v11, v11, v207, v208
	v_med3_f32 v12, v12, v207, v208
	v_med3_f32 v13, v13, v207, v208
	v_med3_f32 v14, v14, v207, v208
	v_med3_f32 v15, v15, v207, v208
	v_med3_f32 v16, v16, v209, v210
	v_med3_f32 v17, v17, v209, v210
	v_med3_f32 v18, v18, v209, v210
	v_med3_f32 v19, v19, v209, v210
	v_med3_f32 v20, v20, v209, v210
	v_med3_f32 v21, v21, v209, v210
	v_med3_f32 v22, v22, v209, v210
	v_med3_f32 v23, v23, v209, v210
	v_med3_f32 v24, v24, v209, v210
	v_med3_f32 v25, v25, v209, v210
	v_med3_f32 v26, v26, v209, v210
	v_med3_f32 v27, v27, v209, v210
	v_med3_f32 v28, v28, v209, v210
	v_med3_f32 v29, v29, v209, v210
	v_med3_f32 v30, v30, v209, v210
	v_med3_f32 v31, v31, v209, v210
	v_med3_f32 v32, v32, v212, v213
	v_med3_f32 v33, v33, v212, v213
	v_med3_f32 v34, v34, v212, v213
	v_med3_f32 v35, v35, v212, v213
	v_med3_f32 v36, v36, v212, v213
	v_med3_f32 v37, v37, v212, v213
	v_med3_f32 v38, v38, v212, v213
	v_med3_f32 v39, v39, v212, v213
	v_med3_f32 v40, v40, v212, v213
	v_med3_f32 v41, v41, v212, v213
	v_med3_f32 v42, v42, v212, v213
	v_med3_f32 v43, v43, v212, v213
	v_med3_f32 v44, v44, v212, v213
	v_med3_f32 v45, v45, v212, v213
	v_med3_f32 v46, v46, v212, v213
	v_med3_f32 v47, v47, v212, v213
	v_med3_f32 v48, v48, v214, v215
	v_med3_f32 v49, v49, v214, v215
	v_med3_f32 v50, v50, v214, v215
	v_med3_f32 v51, v51, v214, v215
	v_med3_f32 v52, v52, v214, v215
	v_med3_f32 v53, v53, v214, v215
	v_med3_f32 v54, v54, v214, v215
	v_med3_f32 v55, v55, v214, v215
	v_med3_f32 v56, v56, v214, v215
	v_med3_f32 v57, v57, v214, v215
	v_med3_f32 v58, v58, v214, v215
	v_med3_f32 v59, v59, v214, v215
	v_med3_f32 v60, v60, v214, v215
	v_med3_f32 v61, v61, v214, v215
	v_med3_f32 v62, v62, v214, v215
	v_med3_f32 v63, v63, v214, v215
	v_add_f32_e32 v0, v0, v16
	v_add_f32_e32 v32, v32, v48
	v_add_f32_e32 v234, v0, v32
	v_add_f32_e32 v1, v1, v17
	v_add_f32_e32 v33, v33, v49
	v_add_f32_e32 v235, v1, v33
	v_add_f32_e32 v2, v2, v18
	v_add_f32_e32 v34, v34, v50
	v_add_f32_e32 v236, v2, v34
	v_add_f32_e32 v3, v3, v19
	v_add_f32_e32 v35, v35, v51
	v_add_f32_e32 v237, v3, v35
	v_add_f32_e32 v4, v4, v20
	v_add_f32_e32 v36, v36, v52
	v_add_f32_e32 v238, v4, v36
	v_add_f32_e32 v5, v5, v21
	v_add_f32_e32 v37, v37, v53
	v_add_f32_e32 v239, v5, v37
	v_add_f32_e32 v6, v6, v22
; #define LAS __attribute__((address_space(3)))
; __device__ __forceinline__ int crow(int reg, int h) { return (reg & 3) + 8 * (reg >> 2) + 4 * h; }
; template <int STAGE>
; __device__ __forceinline__ void pass2(LAS unsigned char* lds, const bf16* kbase, int g, int t0, const bf16x8 (&qf)[4][4], const f32x4 lo4, const f32x4 hi4, int wave, int r, int h2) {
;     ...
;         for (int rg = 0; rg < 16; ++rg) {
;             const int c0 = att::crow(rg, 0);
;             float sv = fsum4_s(__builtin_amdgcn_fmed3f(acc[0][rg], lo4.x, hi4.x), __builtin_amdgcn_fmed3f(acc[1][rg], lo4.y, hi4.y),
;                                __builtin_amdgcn_fmed3f(acc[2][rg], lo4.z, hi4.z), __builtin_amdgcn_fmed3f(acc[3][rg], lo4.w, hi4.w));
;             const int b = bin2(sv, zi);
;             const bool valid = !DIAG || c0 <= lim;
;             if (STAGE == 0) {
;                 atomicAdd((unsigned*)&hist[r * HROW2 + (valid ? b : NB2)], 1u);
;             } else {
;                 if (valid && b > tb) gtw |= 1u << c0;
;                 if (valid && b == tb) eqw |= 1u << c0;
;                 svq[rg] = sv;
;             }
;         }
;         if (STAGE == 1) {
;             LAS unsigned char* st = lds + OFF2_SV + wave * 4096 + (r + 32 * h2) * 16;
; #pragma unroll
;             for (int q = 0; q < 4; ++q) *(LAS f32x4*)(st + q * 1024) = (f32x4){svq[4 * q], svq[4 * q + 1], svq[4 * q + 2], svq[4 * q + 3]};
	v_add_f32_e32 v38, v38, v54
	v_add_f32_e32 v240, v6, v38
	v_add_f32_e32 v7, v7, v23
	v_add_f32_e32 v39, v39, v55
	v_add_f32_e32 v241, v7, v39
	v_add_f32_e32 v8, v8, v24
	v_add_f32_e32 v40, v40, v56
	v_add_f32_e32 v242, v8, v40
	v_add_f32_e32 v9, v9, v25
	v_add_f32_e32 v41, v41, v57
	v_add_f32_e32 v243, v9, v41
	v_add_f32_e32 v10, v10, v26
	v_add_f32_e32 v42, v42, v58
	v_add_f32_e32 v244, v10, v42
	v_add_f32_e32 v11, v11, v27
	v_add_f32_e32 v43, v43, v59
	v_add_f32_e32 v245, v11, v43
	v_add_f32_e32 v12, v12, v28
	v_add_f32_e32 v44, v44, v60
	v_add_f32_e32 v246, v12, v44
	v_add_f32_e32 v13, v13, v29
	v_add_f32_e32 v45, v45, v61
	v_add_f32_e32 v247, v13, v45
	v_add_f32_e32 v14, v14, v30
	v_add_f32_e32 v46, v46, v62
	v_add_f32_e32 v248, v14, v46
	v_add_f32_e32 v15, v15, v31
	v_add_f32_e32 v47, v47, v63
	v_add_f32_e32 v249, v15, v47
	v_cmp_ge_f32_e32 vcc, v234, v250
	v_cmp_ge_f32_e64 s[98:99], v234, v251
	v_cmp_ge_f32_e64 s[100:101], v235, v250
	v_cndmask_b32_e64 v0, 0, 1, vcc
	v_cmp_ge_f32_e32 vcc, v235, v251
	v_cndmask_b32_e64 v16, 0, 1, s[98:99]
	v_cmp_ge_f32_e64 s[98:99], v236, v250
	v_cndmask_b32_e64 v1, 0, 2, s[100:101]
	v_cmp_ge_f32_e64 s[100:101], v236, v251
	v_cndmask_b32_e64 v17, 0, 2, vcc
	v_cmp_ge_f32_e32 vcc, v237, v250
	v_cndmask_b32_e64 v2, 0, 4, s[98:99]
	v_cmp_ge_f32_e64 s[98:99], v237, v251
	v_cndmask_b32_e64 v18, 0, 4, s[100:101]
	v_cmp_ge_f32_e64 s[100:101], v238, v250
	v_cndmask_b32_e64 v3, 0, 8, vcc
	v_cmp_ge_f32_e32 vcc, v238, v251
	v_cndmask_b32_e64 v19, 0, 8, s[98:99]
	v_cmp_ge_f32_e64 s[98:99], v239, v250
	v_cndmask_b32_e64 v4, 0, v186, s[100:101]
	v_cmp_ge_f32_e64 s[100:101], v239, v251
	v_cndmask_b32_e64 v20, 0, v186, vcc
	v_cmp_ge_f32_e32 vcc, v240, v250
	v_cndmask_b32_e64 v5, 0, v193, s[98:99]
	v_cmp_ge_f32_e64 s[98:99], v240, v251
	v_cndmask_b32_e64 v21, 0, v193, s[100:101]
	v_cmp_ge_f32_e64 s[100:101], v241, v250
	v_cndmask_b32_e64 v6, 0, v194, vcc
	v_cmp_ge_f32_e32 vcc, v241, v251
	v_cndmask_b32_e64 v22, 0, v194, s[98:99]
	v_cmp_ge_f32_e64 s[98:99], v242, v250
	v_cndmask_b32_e64 v7, 0, v195, s[100:101]
	v_cmp_ge_f32_e64 s[100:101], v242, v251
	v_cndmask_b32_e64 v23, 0, v195, vcc
	v_cmp_ge_f32_e32 vcc, v243, v250
	v_cndmask_b32_e64 v8, 0, v196, s[98:99]
	v_cmp_ge_f32_e64 s[98:99], v243, v251
	v_cndmask_b32_e64 v24, 0, v196, s[100:101]
	v_cmp_ge_f32_e64 s[100:101], v244, v250
	v_cndmask_b32_e64 v9, 0, v197, vcc
	v_cmp_ge_f32_e32 vcc, v244, v251
	v_cndmask_b32_e64 v25, 0, v197, s[98:99]
	v_cmp_ge_f32_e64 s[98:99], v245, v250
	v_cndmask_b32_e64 v10, 0, v198, s[100:101]
	v_cmp_ge_f32_e64 s[100:101], v245, v251
	v_cndmask_b32_e64 v26, 0, v198, vcc
	v_cmp_ge_f32_e32 vcc, v246, v250
	v_cndmask_b32_e64 v11, 0, v199, s[98:99]
	v_cmp_ge_f32_e64 s[98:99], v246, v251
	v_cndmask_b32_e64 v27, 0, v199, s[100:101]
	v_cmp_ge_f32_e64 s[100:101], v247, v250
	v_cndmask_b32_e64 v12, 0, v200, vcc
	v_cmp_ge_f32_e32 vcc, v247, v251
	v_cndmask_b32_e64 v28, 0, v200, s[98:99]
	v_cmp_ge_f32_e64 s[98:99], v248, v250
	v_cndmask_b32_e64 v13, 0, v201, s[100:101]
	v_cmp_ge_f32_e64 s[100:101], v248, v251
	v_cndmask_b32_e64 v29, 0, v201, vcc
	v_cmp_ge_f32_e32 vcc, v249, v250
	v_cndmask_b32_e64 v14, 0, v202, s[98:99]
	v_cmp_ge_f32_e64 s[98:99], v249, v251
	v_cndmask_b32_e64 v30, 0, v202, s[100:101]
	v_cndmask_b32_e64 v15, 0, v203, vcc
	v_cndmask_b32_e64 v31, 0, v203, s[98:99]
	v_or3_b32 v0, v0, v1, v2
	v_or3_b32 v0, v0, v3, v4
	v_or3_b32 v0, v0, v5, v6
	v_or3_b32 v0, v0, v7, v8
	v_or3_b32 v0, v0, v9, v10
	v_or3_b32 v0, v0, v11, v12
	v_or3_b32 v0, v0, v13, v14
	v_or_b32_e32 v0, v0, v15
	v_or3_b32 v17, v17, v16, v18
	v_or3_b32 v17, v17, v19, v20
	v_or3_b32 v17, v17, v21, v22
	v_or3_b32 v17, v17, v23, v24
	v_or3_b32 v17, v17, v25, v26
	v_or3_b32 v17, v17, v27, v28
	v_or3_b32 v17, v17, v29, v30
	v_or_b32_e32 v17, v17, v31
	v_not_b32_e32 v16, v0
	v_and_b32_e32 v17, v17, v16
	s_waitcnt lgkmcnt(0)
	ds_write_b128 v223, v[234:237]
	ds_write_b128 v223, v[238:241] offset:1024
	ds_write_b128 v223, v[242:245] offset:2048
	ds_write_b128 v223, v[246:249] offset:3072
	v_add_u32_e32 v15, s6, v219
	s_branch .LBB0_830

; __device__ __forceinline__ int crow(int reg, int h) { return (reg & 3) + 8 * (reg >> 2) + 4 * h; }
; #define DSA2_LOADK(dst, kt_) do { _Pragma("unroll") for (int s = 0; s < 4; ++s) dst[s] = *(const bf16x8*)(kp + (size_t)(32 * (kt_)) * Y0P + 16 * s); } while (0)
; template <int STAGE>
; __device__ __forceinline__ void pass2(LAS unsigned char* lds, const bf16* kbase, int g, int t0, const bf16x8 (&qf)[4][4], const f32x4 lo4, const f32x4 hi4, int wave, int r, int h2) {
;     ...
;         f32x16 acc[4];
; #pragma unroll
;         for (int hd = 0; hd < 4; ++hd) {
;             acc[hd] = f32x16{};
; #pragma unroll
;             for (int s = 0; s < 4; ++s) acc[hd] = __builtin_amdgcn_mfma_f32_32x32x16_bf16(WN ? kn[s] : kf[s], qf[hd][s], acc[hd], 0, 0, 0);
;         }
;         const int zi = (8191 - 32 * kt) >> 7;
;         const int lim = tq - 32 * kt - 4 * h2;
;         unsigned gtw = 0u, eqw = 0u;
;         float svq[16];
; #pragma unroll
;         for (int rg = 0; rg < 16; ++rg) {
;             const int c0 = att::crow(rg, 0);
;             float sv = fsum4_s(__builtin_amdgcn_fmed3f(acc[0][rg], lo4.x, hi4.x), __builtin_amdgcn_fmed3f(acc[1][rg], lo4.y, hi4.y),
;                                __builtin_amdgcn_fmed3f(acc[2][rg], lo4.z, hi4.z), __builtin_amdgcn_fmed3f(acc[3][rg], lo4.w, hi4.w));
;     ...
;             gtw <<= 4 * h2;
;             { auto rr = __builtin_amdgcn_permlane32_swap(gtw, gtw, false, false); gtw = rr[0] | rr[1]; }
;             if (h2 == 0) gtm[r * HROW + kt] = gtw;
;         }
;     };
;     ...
;     int kt = wave;
;     if (kt <= g) DSA2_LOADK(kf, kt);
;     for (;;) {
;         if (kt > g) break;
;         if (kt + 8 <= g) DSA2_LOADK(kn, kt + 8);
;         if (kt == g) { tile(pg8::BoolC2<false>{}, kt, pg8::BoolC2<true>{}); break; }
;         tile(pg8::BoolC2<false>{}, kt, pg8::BoolC2<false>{});
;         kt += 8;
;         if (kt > g) break;
;         if (kt + 8 <= g) DSA2_LOADK(kf, kt + 8);
;         if (kt == g) { tile(pg8::BoolC2<true>{}, kt, pg8::BoolC2<true>{}); break; }
;         tile(pg8::BoolC2<true>{}, kt, pg8::BoolC2<false>{});
.LBB0_834:
.LBB0_835:
	v_lshlrev_b32_e32 v0, v219, v0
	v_mov_b32_e32 v1, v0
	s_nop 1
	v_permlane32_swap_b32_e32 v0, v1
	s_and_saveexec_b64 s[6:7], s[84:85]
	v_or_b32_e32 v0, v0, v1
	v_lshl_add_u32 v1, s0, 2, v217
	ds_write_b32 v1, v0
	s_or_b64 exec, exec, s[6:7]
	s_mov_b64 s[6:7], -1
	s_andn2_b64 vcc, exec, s[4:5]
	s_mov_b64 s[4:5], -1
	s_cbranch_vccnz .LBB0_854
	s_add_i32 s10, s0, 16
	s_cmp_gt_u32 s10, s64
	s_cselect_b64 s[4:5], -1, 0
	v_mov_b64_e32 v[174:175], v[130:131]
	v_mov_b64_e32 v[170:171], v[134:135]
	v_mov_b64_e32 v[166:167], v[138:139]
	v_mov_b64_e32 v[162:163], v[142:143]
	s_and_b64 vcc, exec, s[4:5]
	v_mov_b64_e32 v[172:173], v[128:129]
	v_mov_b64_e32 v[168:169], v[132:133]
	v_mov_b64_e32 v[164:165], v[136:137]
	v_mov_b64_e32 v[160:161], v[140:141]
	s_cbranch_vccnz .LBB0_840
	s_lshl_b32 s6, s10, 5
	v_mad_u64_u32 v[0:1], s[6:7], s6, v187, v[178:179]
	global_load_dwordx4 v[160:163], v[0:1], off
	global_load_dwordx4 v[164:167], v[0:1], off offset:32
	global_load_dwordx4 v[168:171], v[0:1], off offset:64
	global_load_dwordx4 v[172:175], v[0:1], off offset:96
.LBB0_840:
	s_cmp_lg_u32 s1, s64
	s_cbranch_scc0 .LBB0_853
	v_mfma_f32_32x32x16_bf16 v[0:15], v[156:159], v[64:67], 0
	s_lshl_b32 s1, s1, 5
	s_sub_i32 s6, 0x1fe0, s1
	s_lshr_b32 s6, s6, 7
	s_addk_i32 s6, 0xd0
	v_mfma_f32_32x32x16_bf16 v[16:31], v[156:159], v[80:83], 0
	v_mfma_f32_32x32x16_bf16 v[32:47], v[156:159], v[96:99], 0
	v_mfma_f32_32x32x16_bf16 v[48:63], v[156:159], v[112:115], 0
	v_mfma_f32_32x32x16_bf16 v[0:15], v[152:155], v[68:71], v[0:15]
	v_mfma_f32_32x32x16_bf16 v[16:31], v[152:155], v[84:87], v[16:31]
	v_mfma_f32_32x32x16_bf16 v[32:47], v[152:155], v[100:103], v[32:47]
	v_mfma_f32_32x32x16_bf16 v[48:63], v[152:155], v[116:119], v[48:63]
	v_mfma_f32_32x32x16_bf16 v[0:15], v[148:151], v[72:75], v[0:15]
	v_mfma_f32_32x32x16_bf16 v[16:31], v[148:151], v[88:91], v[16:31]
	v_mfma_f32_32x32x16_bf16 v[32:47], v[148:151], v[104:107], v[32:47]
	v_mfma_f32_32x32x16_bf16 v[48:63], v[148:151], v[120:123], v[48:63]
	v_mfma_f32_32x32x16_bf16 v[0:15], v[144:147], v[76:79], v[0:15]
	v_mfma_f32_32x32x16_bf16 v[16:31], v[144:147], v[92:95], v[16:31]
	v_mfma_f32_32x32x16_bf16 v[32:47], v[144:147], v[108:111], v[32:47]
	v_mfma_f32_32x32x16_bf16 v[48:63], v[144:147], v[124:127], v[48:63]
	v_cmp_gt_i32_e32 vcc, s6, v232
	v_cmp_ge_i32_e64 s[98:99], s6, v232
	s_nop 6
	v_cndmask_b32_e32 v250, v252, v177, vcc
	v_cndmask_b32_e64 v251, v253, v177, s[98:99]
	v_med3_f32 v0, v0, v207, v208
	v_med3_f32 v1, v1, v207, v208
	v_med3_f32 v2, v2, v207, v208
	v_med3_f32 v3, v3, v207, v208
	v_med3_f32 v4, v4, v207, v208
	v_med3_f32 v5, v5, v207, v208
	v_med3_f32 v6, v6, v207, v208
	v_med3_f32 v7, v7, v207, v208
	v_med3_f32 v8, v8, v207, v208
	v_med3_f32 v9, v9, v207, v208
	v_med3_f32 v10, v10, v207, v208
	v_med3_f32 v11, v11, v207, v208
	v_med3_f32 v12, v12, v207, v208
	v_med3_f32 v13, v13, v207, v208
	v_med3_f32 v14, v14, v207, v208
	v_med3_f32 v15, v15, v207, v208
	v_med3_f32 v16, v16, v209, v210
	v_med3_f32 v17, v17, v209, v210
	v_med3_f32 v18, v18, v209, v210
	v_med3_f32 v19, v19, v209, v210
	v_med3_f32 v20, v20, v209, v210
	v_med3_f32 v21, v21, v209, v210
	v_med3_f32 v22, v22, v209, v210
	v_med3_f32 v23, v23, v209, v210
	v_med3_f32 v24, v24, v209, v210
	v_med3_f32 v25, v25, v209, v210
	v_med3_f32 v26, v26, v209, v210
	v_med3_f32 v27, v27, v209, v210
	v_med3_f32 v28, v28, v209, v210
	v_med3_f32 v29, v29, v209, v210
	v_med3_f32 v30, v30, v209, v210
	v_med3_f32 v31, v31, v209, v210
	v_med3_f32 v32, v32, v212, v213
	v_med3_f32 v33, v33, v212, v213
	v_med3_f32 v34, v34, v212, v213
	v_med3_f32 v35, v35, v212, v213
	v_med3_f32 v36, v36, v212, v213
	v_med3_f32 v37, v37, v212, v213
	v_med3_f32 v38, v38, v212, v213
	v_med3_f32 v39, v39, v212, v213
	v_med3_f32 v40, v40, v212, v213
	v_med3_f32 v41, v41, v212, v213
	v_med3_f32 v42, v42, v212, v213
	v_med3_f32 v43, v43, v212, v213
	v_med3_f32 v44, v44, v212, v213
	v_med3_f32 v45, v45, v212, v213
	v_med3_f32 v46, v46, v212, v213
	v_med3_f32 v47, v47, v212, v213
	v_med3_f32 v48, v48, v214, v215
	v_med3_f32 v49, v49, v214, v215
	v_med3_f32 v50, v50, v214, v215
	v_med3_f32 v51, v51, v214, v215
	v_med3_f32 v52, v52, v214, v215
	v_med3_f32 v53, v53, v214, v215
	v_med3_f32 v54, v54, v214, v215
	v_med3_f32 v55, v55, v214, v215
	v_med3_f32 v56, v56, v214, v215
	v_med3_f32 v57, v57, v214, v215
	v_med3_f32 v58, v58, v214, v215
	v_med3_f32 v59, v59, v214, v215
	v_med3_f32 v60, v60, v214, v215
	v_med3_f32 v61, v61, v214, v215
	v_med3_f32 v62, v62, v214, v215
	v_med3_f32 v63, v63, v214, v215
	v_add_f32_e32 v0, v0, v16
; #define LAS __attribute__((address_space(3)))
; __device__ __forceinline__ int crow(int reg, int h) { return (reg & 3) + 8 * (reg >> 2) + 4 * h; }
; template <int STAGE>
; __device__ __forceinline__ void pass2(LAS unsigned char* lds, const bf16* kbase, int g, int t0, const bf16x8 (&qf)[4][4], const f32x4 lo4, const f32x4 hi4, int wave, int r, int h2) {
;     ...
;         for (int rg = 0; rg < 16; ++rg) {
;             const int c0 = att::crow(rg, 0);
;             float sv = fsum4_s(__builtin_amdgcn_fmed3f(acc[0][rg], lo4.x, hi4.x), __builtin_amdgcn_fmed3f(acc[1][rg], lo4.y, hi4.y),
;                                __builtin_amdgcn_fmed3f(acc[2][rg], lo4.z, hi4.z), __builtin_amdgcn_fmed3f(acc[3][rg], lo4.w, hi4.w));
;             const int b = bin2(sv, zi);
;             const bool valid = !DIAG || c0 <= lim;
;             if (STAGE == 0) {
;                 atomicAdd((unsigned*)&hist[r * HROW2 + (valid ? b : NB2)], 1u);
;             } else {
;                 if (valid && b > tb) gtw |= 1u << c0;
;                 if (valid && b == tb) eqw |= 1u << c0;
;                 svq[rg] = sv;
;             }
;         }
;         if (STAGE == 1) {
;             LAS unsigned char* st = lds + OFF2_SV + wave * 4096 + (r + 32 * h2) * 16;
; #pragma unroll
;             for (int q = 0; q < 4; ++q) *(LAS f32x4*)(st + q * 1024) = (f32x4){svq[4 * q], svq[4 * q + 1], svq[4 * q + 2], svq[4 * q + 3]};
	v_add_f32_e32 v32, v32, v48
	v_add_f32_e32 v234, v0, v32
	v_add_f32_e32 v1, v1, v17
	v_add_f32_e32 v33, v33, v49
	v_add_f32_e32 v235, v1, v33
	v_add_f32_e32 v2, v2, v18
	v_add_f32_e32 v34, v34, v50
	v_add_f32_e32 v236, v2, v34
	v_add_f32_e32 v3, v3, v19
	v_add_f32_e32 v35, v35, v51
	v_add_f32_e32 v237, v3, v35
	v_add_f32_e32 v4, v4, v20
	v_add_f32_e32 v36, v36, v52
	v_add_f32_e32 v238, v4, v36
	v_add_f32_e32 v5, v5, v21
	v_add_f32_e32 v37, v37, v53
	v_add_f32_e32 v239, v5, v37
	v_add_f32_e32 v6, v6, v22
	v_add_f32_e32 v38, v38, v54
	v_add_f32_e32 v240, v6, v38
	v_add_f32_e32 v7, v7, v23
	v_add_f32_e32 v39, v39, v55
	v_add_f32_e32 v241, v7, v39
	v_add_f32_e32 v8, v8, v24
	v_add_f32_e32 v40, v40, v56
	v_add_f32_e32 v242, v8, v40
	v_add_f32_e32 v9, v9, v25
	v_add_f32_e32 v41, v41, v57
	v_add_f32_e32 v243, v9, v41
	v_add_f32_e32 v10, v10, v26
	v_add_f32_e32 v42, v42, v58
	v_add_f32_e32 v244, v10, v42
	v_add_f32_e32 v11, v11, v27
	v_add_f32_e32 v43, v43, v59
	v_add_f32_e32 v245, v11, v43
	v_add_f32_e32 v12, v12, v28
	v_add_f32_e32 v44, v44, v60
	v_add_f32_e32 v246, v12, v44
	v_add_f32_e32 v13, v13, v29
	v_add_f32_e32 v45, v45, v61
	v_add_f32_e32 v247, v13, v45
	v_add_f32_e32 v14, v14, v30
	v_add_f32_e32 v46, v46, v62
	v_add_f32_e32 v248, v14, v46
	v_add_f32_e32 v15, v15, v31
	v_add_f32_e32 v47, v47, v63
	v_add_f32_e32 v249, v15, v47
	v_cmp_ge_f32_e32 vcc, v234, v250
	v_cmp_ge_f32_e64 s[98:99], v234, v251
	v_cmp_ge_f32_e64 s[100:101], v235, v250
	v_cndmask_b32_e64 v0, 0, 1, vcc
	v_cmp_ge_f32_e32 vcc, v235, v251
	v_cndmask_b32_e64 v16, 0, 1, s[98:99]
	v_cmp_ge_f32_e64 s[98:99], v236, v250
	v_cndmask_b32_e64 v1, 0, 2, s[100:101]
	v_cmp_ge_f32_e64 s[100:101], v236, v251
	v_cndmask_b32_e64 v17, 0, 2, vcc
	v_cmp_ge_f32_e32 vcc, v237, v250
	v_cndmask_b32_e64 v2, 0, 4, s[98:99]
	v_cmp_ge_f32_e64 s[98:99], v237, v251
	v_cndmask_b32_e64 v18, 0, 4, s[100:101]
	v_cmp_ge_f32_e64 s[100:101], v238, v250
	v_cndmask_b32_e64 v3, 0, 8, vcc
	v_cmp_ge_f32_e32 vcc, v238, v251
	v_cndmask_b32_e64 v19, 0, 8, s[98:99]
	v_cmp_ge_f32_e64 s[98:99], v239, v250
	v_cndmask_b32_e64 v4, 0, v186, s[100:101]
	v_cmp_ge_f32_e64 s[100:101], v239, v251
	v_cndmask_b32_e64 v20, 0, v186, vcc
	v_cmp_ge_f32_e32 vcc, v240, v250
	v_cndmask_b32_e64 v5, 0, v193, s[98:99]
	v_cmp_ge_f32_e64 s[98:99], v240, v251
	v_cndmask_b32_e64 v21, 0, v193, s[100:101]
	v_cmp_ge_f32_e64 s[100:101], v241, v250
	v_cndmask_b32_e64 v6, 0, v194, vcc
	v_cmp_ge_f32_e32 vcc, v241, v251
	v_cndmask_b32_e64 v22, 0, v194, s[98:99]
	v_cmp_ge_f32_e64 s[98:99], v242, v250
	v_cndmask_b32_e64 v7, 0, v195, s[100:101]
	v_cmp_ge_f32_e64 s[100:101], v242, v251
	v_cndmask_b32_e64 v23, 0, v195, vcc
	v_cmp_ge_f32_e32 vcc, v243, v250
	v_cndmask_b32_e64 v8, 0, v196, s[98:99]
	v_cmp_ge_f32_e64 s[98:99], v243, v251
	v_cndmask_b32_e64 v24, 0, v196, s[100:101]
	v_cmp_ge_f32_e64 s[100:101], v244, v250
	v_cndmask_b32_e64 v9, 0, v197, vcc
	v_cmp_ge_f32_e32 vcc, v244, v251
	v_cndmask_b32_e64 v25, 0, v197, s[98:99]
	v_cmp_ge_f32_e64 s[98:99], v245, v250
	v_cndmask_b32_e64 v10, 0, v198, s[100:101]
	v_cmp_ge_f32_e64 s[100:101], v245, v251
	v_cndmask_b32_e64 v26, 0, v198, vcc
	v_cmp_ge_f32_e32 vcc, v246, v250
	v_cndmask_b32_e64 v11, 0, v199, s[98:99]
	v_cmp_ge_f32_e64 s[98:99], v246, v251
	v_cndmask_b32_e64 v27, 0, v199, s[100:101]
	v_cmp_ge_f32_e64 s[100:101], v247, v250
	v_cndmask_b32_e64 v12, 0, v200, vcc
	v_cmp_ge_f32_e32 vcc, v247, v251
	v_cndmask_b32_e64 v28, 0, v200, s[98:99]
	v_cmp_ge_f32_e64 s[98:99], v248, v250
	v_cndmask_b32_e64 v13, 0, v201, s[100:101]
	v_cmp_ge_f32_e64 s[100:101], v248, v251
	v_cndmask_b32_e64 v29, 0, v201, vcc
	v_cmp_ge_f32_e32 vcc, v249, v250
	v_cndmask_b32_e64 v14, 0, v202, s[98:99]
	v_cmp_ge_f32_e64 s[98:99], v249, v251
	v_cndmask_b32_e64 v30, 0, v202, s[100:101]
	v_cndmask_b32_e64 v15, 0, v203, vcc
	v_cndmask_b32_e64 v31, 0, v203, s[98:99]
	v_or3_b32 v0, v0, v1, v2
	v_or3_b32 v0, v0, v3, v4
	v_or3_b32 v0, v0, v5, v6
	v_or3_b32 v0, v0, v7, v8
	v_or3_b32 v0, v0, v9, v10
	v_or3_b32 v0, v0, v11, v12
	v_or3_b32 v0, v0, v13, v14
	v_or_b32_e32 v0, v0, v15
	v_or3_b32 v17, v17, v16, v18
	v_or3_b32 v17, v17, v19, v20
	v_or3_b32 v17, v17, v21, v22
	v_or3_b32 v17, v17, v23, v24
	v_or3_b32 v17, v17, v25, v26
	v_or3_b32 v17, v17, v27, v28
	v_or3_b32 v17, v17, v29, v30
	v_or_b32_e32 v17, v17, v31
	v_not_b32_e32 v16, v0
	v_and_b32_e32 v17, v17, v16
	s_waitcnt lgkmcnt(0)
	ds_write_b128 v223, v[234:237]
	ds_write_b128 v223, v[238:241] offset:1024
	ds_write_b128 v223, v[242:245] offset:2048
	ds_write_b128 v223, v[246:249] offset:3072
	v_add_u32_e32 v15, s1, v219
	s_branch .LBB0_844

; template <int STAGE>
; __device__ __forceinline__ void pass2(LAS unsigned char* lds, const bf16* kbase, int g, int t0, const bf16x8 (&qf)[4][4], const f32x4 lo4, const f32x4 hi4, int wave, int r, int h2) {
;     ...
;             gtw <<= 4 * h2;
;             { auto rr = __builtin_amdgcn_permlane32_swap(gtw, gtw, false, false); gtw = rr[0] | rr[1]; }
;             if (h2 == 0) gtm[r * HROW + kt] = gtw;
;         }
.LBB0_848:
.LBB0_849:
	v_lshlrev_b32_e32 v0, v219, v0
	v_mov_b32_e32 v1, v0
	s_nop 1
	v_permlane32_swap_b32_e32 v0, v1
	s_and_saveexec_b64 s[6:7], s[84:85]
	v_or_b32_e32 v0, v0, v1
	v_lshl_add_u32 v1, s0, 2, v217
	ds_write_b32 v1, v0 offset:32
	s_or_b64 exec, exec, s[6:7]
	s_mov_b64 s[6:7], -1
	s_branch .LBB0_854
